# in_proj epilogue: dedicated straight-line paths per tile kind (sigmoid gate tiles: packed scale and +1 in place in the accumulators; plain tiles convert directly), original select code kept for the q/
# baseline (speedup 1.0000x reference)
.LBB0_185:
	s_cmp_gt_i32 s6, 21
	s_cbranch_scc1 .Lepi_sig_0
	s_cmp_gt_i32 s6, 1
	s_cbranch_scc1 .Lepi_plain_0
	s_cmp_gt_i32 s6, 1
	v_pk_mul_f32 v[128:129], v[60:61], s[30:31] op_sel_hi:[1,0]
	s_cselect_b64 s[4:5], -1, 0
	s_cmp_lt_i32 s6, 22
	v_pk_mul_f32 v[130:131], v[62:63], s[30:31] op_sel_hi:[1,0]
	v_pk_mul_f32 v[152:153], v[58:59], s[30:31] op_sel_hi:[1,0]
	v_pk_mul_f32 v[132:133], v[56:57], s[30:31] op_sel_hi:[1,0]
	s_cselect_b64 s[50:51], -1, 0
	s_cmp_gt_i32 s6, 21
	v_cndmask_b32_e64 v128, v128, v60, s[4:5]
	v_cndmask_b32_e64 v129, v129, v61, s[4:5]
	v_cndmask_b32_e64 v130, v130, v62, s[4:5]
	v_cndmask_b32_e64 v135, v131, v63, s[4:5]
	v_cndmask_b32_e64 v132, v132, v56, s[4:5]
	v_cndmask_b32_e64 v133, v133, v57, s[4:5]
	v_cndmask_b32_e64 v134, v152, v58, s[4:5]
	v_cndmask_b32_e64 v131, v153, v59, s[4:5]
	s_mov_b64 s[52:53], -1
	s_cbranch_scc1 .LBB0_187
	s_mov_b64 s[52:53], 0

.Lepi_sig_0:
	v_lshl_or_b32 v152, s6, 8, v162
	v_mov_b64_e32 v[154:155], s[12:13]
	v_ashrrev_i32_e32 v153, 31, v152
	v_mad_i64_i32 v[154:155], s[6:7], v150, s68, v[154:155]
	v_lshl_add_u64 v[154:155], v[152:153], 1, v[154:155]
	s_mov_b32 s50, 0xbfb8aa3b
	s_mov_b32 s52, 1.0
	v_pk_mul_f32 v[56:57], v[56:57], s[50:51] op_sel_hi:[1,0]
	v_pk_mul_f32 v[58:59], v[58:59], s[50:51] op_sel_hi:[1,0]
	v_pk_mul_f32 v[60:61], v[60:61], s[50:51] op_sel_hi:[1,0]
	v_pk_mul_f32 v[62:63], v[62:63], s[50:51] op_sel_hi:[1,0]
	v_exp_f32_e32 v56, v56
	v_exp_f32_e32 v57, v57
	v_exp_f32_e32 v58, v58
	v_exp_f32_e32 v59, v59
	v_exp_f32_e32 v60, v60
	v_exp_f32_e32 v61, v61
	v_exp_f32_e32 v62, v62
	v_exp_f32_e32 v63, v63
	v_pk_add_f32 v[56:57], v[56:57], s[52:53] op_sel_hi:[1,0]
	v_pk_add_f32 v[58:59], v[58:59], s[52:53] op_sel_hi:[1,0]
	v_pk_add_f32 v[60:61], v[60:61], s[52:53] op_sel_hi:[1,0]
	v_pk_add_f32 v[62:63], v[62:63], s[52:53] op_sel_hi:[1,0]
	v_rcp_f32_e32 v56, v56
	v_rcp_f32_e32 v57, v57
	v_rcp_f32_e32 v58, v58
	v_rcp_f32_e32 v59, v59
	v_rcp_f32_e32 v60, v60
	v_rcp_f32_e32 v61, v61
	v_rcp_f32_e32 v62, v62
	v_rcp_f32_e32 v63, v63
	s_nop 0
	v_cvt_pk_bf16_f32 v128, v60, v61
	v_cvt_pk_bf16_f32 v129, v62, v63
	v_cvt_pk_bf16_f32 v130, v56, v57
	v_cvt_pk_bf16_f32 v131, v58, v59
	global_store_dwordx4 v[154:155], v[128:131], off
	s_nop 1
	s_mov_b32 s50, 0xbfb8aa3b
	s_mov_b32 s52, 1.0
	v_pk_mul_f32 v[120:121], v[120:121], s[50:51] op_sel_hi:[1,0]
	v_pk_mul_f32 v[122:123], v[122:123], s[50:51] op_sel_hi:[1,0]
	v_pk_mul_f32 v[124:125], v[124:125], s[50:51] op_sel_hi:[1,0]
	v_pk_mul_f32 v[126:127], v[126:127], s[50:51] op_sel_hi:[1,0]
	v_exp_f32_e32 v120, v120
	v_exp_f32_e32 v121, v121
	v_exp_f32_e32 v122, v122
	v_exp_f32_e32 v123, v123
	v_exp_f32_e32 v124, v124
	v_exp_f32_e32 v125, v125
	v_exp_f32_e32 v126, v126
	v_exp_f32_e32 v127, v127
	v_pk_add_f32 v[120:121], v[120:121], s[52:53] op_sel_hi:[1,0]
	v_pk_add_f32 v[122:123], v[122:123], s[52:53] op_sel_hi:[1,0]
	v_pk_add_f32 v[124:125], v[124:125], s[52:53] op_sel_hi:[1,0]
	v_pk_add_f32 v[126:127], v[126:127], s[52:53] op_sel_hi:[1,0]
	v_rcp_f32_e32 v120, v120
	v_rcp_f32_e32 v121, v121
	v_rcp_f32_e32 v122, v122
	v_rcp_f32_e32 v123, v123
	v_rcp_f32_e32 v124, v124
	v_rcp_f32_e32 v125, v125
	v_rcp_f32_e32 v126, v126
	v_rcp_f32_e32 v127, v127
	s_nop 0
	v_cvt_pk_bf16_f32 v124, v124, v125
	v_cvt_pk_bf16_f32 v125, v126, v127
	v_cvt_pk_bf16_f32 v126, v120, v121
	v_cvt_pk_bf16_f32 v127, v122, v123
	global_store_dwordx4 v[154:155], v[124:127], off offset:256
	s_nop 1
	v_or_b32_e32 v130, 16, v150
	v_mov_b64_e32 v[128:129], s[12:13]
	v_mad_i64_i32 v[128:129], s[50:51], v130, s68, v[128:129]
	v_lshl_add_u64 v[128:129], v[152:153], 1, v[128:129]
	s_mov_b32 s50, 0xbfb8aa3b
	s_mov_b32 s52, 1.0
	v_pk_mul_f32 v[48:49], v[48:49], s[50:51] op_sel_hi:[1,0]
	v_pk_mul_f32 v[50:51], v[50:51], s[50:51] op_sel_hi:[1,0]
	v_pk_mul_f32 v[52:53], v[52:53], s[50:51] op_sel_hi:[1,0]
	v_pk_mul_f32 v[54:55], v[54:55], s[50:51] op_sel_hi:[1,0]
	v_exp_f32_e32 v48, v48
	v_exp_f32_e32 v49, v49
	v_exp_f32_e32 v50, v50
	v_exp_f32_e32 v51, v51
	v_exp_f32_e32 v52, v52
	v_exp_f32_e32 v53, v53
	v_exp_f32_e32 v54, v54
	v_exp_f32_e32 v55, v55
	v_pk_add_f32 v[48:49], v[48:49], s[52:53] op_sel_hi:[1,0]
	v_pk_add_f32 v[50:51], v[50:51], s[52:53] op_sel_hi:[1,0]
	v_pk_add_f32 v[52:53], v[52:53], s[52:53] op_sel_hi:[1,0]
	v_pk_add_f32 v[54:55], v[54:55], s[52:53] op_sel_hi:[1,0]
	v_rcp_f32_e32 v48, v48
	v_rcp_f32_e32 v49, v49
	v_rcp_f32_e32 v50, v50
	v_rcp_f32_e32 v51, v51
	v_rcp_f32_e32 v52, v52
	v_rcp_f32_e32 v53, v53
	v_rcp_f32_e32 v54, v54
	v_rcp_f32_e32 v55, v55
	s_nop 0
	v_cvt_pk_bf16_f32 v122, v52, v53
	v_cvt_pk_bf16_f32 v123, v54, v55
	v_cvt_pk_bf16_f32 v124, v48, v49
	v_cvt_pk_bf16_f32 v125, v50, v51
	global_store_dwordx4 v[128:129], v[122:125], off
	s_nop 1
	s_mov_b32 s50, 0xbfb8aa3b
	s_mov_b32 s52, 1.0
	v_pk_mul_f32 v[112:113], v[112:113], s[50:51] op_sel_hi:[1,0]
	v_pk_mul_f32 v[114:115], v[114:115], s[50:51] op_sel_hi:[1,0]
	v_pk_mul_f32 v[116:117], v[116:117], s[50:51] op_sel_hi:[1,0]
	v_pk_mul_f32 v[118:119], v[118:119], s[50:51] op_sel_hi:[1,0]
	v_exp_f32_e32 v112, v112
	v_exp_f32_e32 v113, v113
	v_exp_f32_e32 v114, v114
	v_exp_f32_e32 v115, v115
	v_exp_f32_e32 v116, v116
	v_exp_f32_e32 v117, v117
	v_exp_f32_e32 v118, v118
	v_exp_f32_e32 v119, v119
	v_pk_add_f32 v[112:113], v[112:113], s[52:53] op_sel_hi:[1,0]
	v_pk_add_f32 v[114:115], v[114:115], s[52:53] op_sel_hi:[1,0]
	v_pk_add_f32 v[116:117], v[116:117], s[52:53] op_sel_hi:[1,0]
	v_pk_add_f32 v[118:119], v[118:119], s[52:53] op_sel_hi:[1,0]
	v_rcp_f32_e32 v112, v112
	v_rcp_f32_e32 v113, v113
	v_rcp_f32_e32 v114, v114
	v_rcp_f32_e32 v115, v115
	v_rcp_f32_e32 v116, v116
	v_rcp_f32_e32 v117, v117
	v_rcp_f32_e32 v118, v118
	v_rcp_f32_e32 v119, v119
	s_nop 0
	v_cvt_pk_bf16_f32 v116, v116, v117
	v_cvt_pk_bf16_f32 v117, v118, v119
	v_cvt_pk_bf16_f32 v118, v112, v113
	v_cvt_pk_bf16_f32 v119, v114, v115
	global_store_dwordx4 v[128:129], v[116:119], off offset:256
	s_nop 1
	v_or_b32_e32 v122, 32, v150
	v_mov_b64_e32 v[120:121], s[12:13]
	v_mad_i64_i32 v[120:121], s[50:51], v122, s68, v[120:121]
	v_lshl_add_u64 v[120:121], v[152:153], 1, v[120:121]
	s_mov_b32 s50, 0xbfb8aa3b
	s_mov_b32 s52, 1.0
	v_pk_mul_f32 v[40:41], v[40:41], s[50:51] op_sel_hi:[1,0]
	v_pk_mul_f32 v[42:43], v[42:43], s[50:51] op_sel_hi:[1,0]
	v_pk_mul_f32 v[44:45], v[44:45], s[50:51] op_sel_hi:[1,0]
	v_pk_mul_f32 v[46:47], v[46:47], s[50:51] op_sel_hi:[1,0]
	v_exp_f32_e32 v40, v40
	v_exp_f32_e32 v41, v41
	v_exp_f32_e32 v42, v42
	v_exp_f32_e32 v43, v43
	v_exp_f32_e32 v44, v44
	v_exp_f32_e32 v45, v45
	v_exp_f32_e32 v46, v46
	v_exp_f32_e32 v47, v47
	v_pk_add_f32 v[40:41], v[40:41], s[52:53] op_sel_hi:[1,0]
	v_pk_add_f32 v[42:43], v[42:43], s[52:53] op_sel_hi:[1,0]
	v_pk_add_f32 v[44:45], v[44:45], s[52:53] op_sel_hi:[1,0]
	v_pk_add_f32 v[46:47], v[46:47], s[52:53] op_sel_hi:[1,0]
	v_rcp_f32_e32 v40, v40
	v_rcp_f32_e32 v41, v41
	v_rcp_f32_e32 v42, v42
	v_rcp_f32_e32 v43, v43
	v_rcp_f32_e32 v44, v44
	v_rcp_f32_e32 v45, v45
	v_rcp_f32_e32 v46, v46
	v_rcp_f32_e32 v47, v47
	s_nop 0
	v_cvt_pk_bf16_f32 v114, v44, v45
	v_cvt_pk_bf16_f32 v115, v46, v47
	v_cvt_pk_bf16_f32 v116, v40, v41
	v_cvt_pk_bf16_f32 v117, v42, v43
	global_store_dwordx4 v[120:121], v[114:117], off
	s_nop 1
	s_mov_b32 s50, 0xbfb8aa3b
	s_mov_b32 s52, 1.0
	v_pk_mul_f32 v[104:105], v[104:105], s[50:51] op_sel_hi:[1,0]
	v_pk_mul_f32 v[106:107], v[106:107], s[50:51] op_sel_hi:[1,0]
	v_pk_mul_f32 v[108:109], v[108:109], s[50:51] op_sel_hi:[1,0]
	v_pk_mul_f32 v[110:111], v[110:111], s[50:51] op_sel_hi:[1,0]
	v_exp_f32_e32 v104, v104
	v_exp_f32_e32 v105, v105
	v_exp_f32_e32 v106, v106
	v_exp_f32_e32 v107, v107
	v_exp_f32_e32 v108, v108
	v_exp_f32_e32 v109, v109
	v_exp_f32_e32 v110, v110
	v_exp_f32_e32 v111, v111
	v_pk_add_f32 v[104:105], v[104:105], s[52:53] op_sel_hi:[1,0]
	v_pk_add_f32 v[106:107], v[106:107], s[52:53] op_sel_hi:[1,0]
	v_pk_add_f32 v[108:109], v[108:109], s[52:53] op_sel_hi:[1,0]
	v_pk_add_f32 v[110:111], v[110:111], s[52:53] op_sel_hi:[1,0]
	v_rcp_f32_e32 v104, v104
	v_rcp_f32_e32 v105, v105
	v_rcp_f32_e32 v106, v106
	v_rcp_f32_e32 v107, v107
	v_rcp_f32_e32 v108, v108
	v_rcp_f32_e32 v109, v109
	v_rcp_f32_e32 v110, v110
	v_rcp_f32_e32 v111, v111
	s_nop 0
	v_cvt_pk_bf16_f32 v108, v108, v109
	v_cvt_pk_bf16_f32 v109, v110, v111
	v_cvt_pk_bf16_f32 v110, v104, v105
	v_cvt_pk_bf16_f32 v111, v106, v107
	global_store_dwordx4 v[120:121], v[108:111], off offset:256
	s_nop 1
	v_or_b32_e32 v114, 48, v150
	v_mov_b64_e32 v[112:113], s[12:13]
	v_mad_i64_i32 v[112:113], s[50:51], v114, s68, v[112:113]
	v_lshl_add_u64 v[112:113], v[152:153], 1, v[112:113]
	s_mov_b32 s50, 0xbfb8aa3b
	s_mov_b32 s52, 1.0
	v_pk_mul_f32 v[32:33], v[32:33], s[50:51] op_sel_hi:[1,0]
	v_pk_mul_f32 v[34:35], v[34:35], s[50:51] op_sel_hi:[1,0]
	v_pk_mul_f32 v[36:37], v[36:37], s[50:51] op_sel_hi:[1,0]
	v_pk_mul_f32 v[38:39], v[38:39], s[50:51] op_sel_hi:[1,0]
	v_exp_f32_e32 v32, v32
	v_exp_f32_e32 v33, v33
	v_exp_f32_e32 v34, v34
	v_exp_f32_e32 v35, v35
	v_exp_f32_e32 v36, v36
	v_exp_f32_e32 v37, v37
	v_exp_f32_e32 v38, v38
	v_exp_f32_e32 v39, v39
	v_pk_add_f32 v[32:33], v[32:33], s[52:53] op_sel_hi:[1,0]
	v_pk_add_f32 v[34:35], v[34:35], s[52:53] op_sel_hi:[1,0]
	v_pk_add_f32 v[36:37], v[36:37], s[52:53] op_sel_hi:[1,0]
	v_pk_add_f32 v[38:39], v[38:39], s[52:53] op_sel_hi:[1,0]
	v_rcp_f32_e32 v32, v32
	v_rcp_f32_e32 v33, v33
	v_rcp_f32_e32 v34, v34
	v_rcp_f32_e32 v35, v35
	v_rcp_f32_e32 v36, v36
	v_rcp_f32_e32 v37, v37
	v_rcp_f32_e32 v38, v38
	v_rcp_f32_e32 v39, v39
	s_nop 0
	v_cvt_pk_bf16_f32 v106, v36, v37
	v_cvt_pk_bf16_f32 v107, v38, v39
	v_cvt_pk_bf16_f32 v108, v32, v33
	v_cvt_pk_bf16_f32 v109, v34, v35
	global_store_dwordx4 v[112:113], v[106:109], off
	s_nop 1
	s_mov_b32 s50, 0xbfb8aa3b
	s_mov_b32 s52, 1.0
	v_pk_mul_f32 v[96:97], v[96:97], s[50:51] op_sel_hi:[1,0]
	v_pk_mul_f32 v[98:99], v[98:99], s[50:51] op_sel_hi:[1,0]
	v_pk_mul_f32 v[100:101], v[100:101], s[50:51] op_sel_hi:[1,0]
	v_pk_mul_f32 v[102:103], v[102:103], s[50:51] op_sel_hi:[1,0]
	v_exp_f32_e32 v96, v96
	v_exp_f32_e32 v97, v97
	v_exp_f32_e32 v98, v98
	v_exp_f32_e32 v99, v99
	v_exp_f32_e32 v100, v100
	v_exp_f32_e32 v101, v101
	v_exp_f32_e32 v102, v102
	v_exp_f32_e32 v103, v103
	v_pk_add_f32 v[96:97], v[96:97], s[52:53] op_sel_hi:[1,0]
	v_pk_add_f32 v[98:99], v[98:99], s[52:53] op_sel_hi:[1,0]
	v_pk_add_f32 v[100:101], v[100:101], s[52:53] op_sel_hi:[1,0]
	v_pk_add_f32 v[102:103], v[102:103], s[52:53] op_sel_hi:[1,0]
	v_rcp_f32_e32 v96, v96
	v_rcp_f32_e32 v97, v97
	v_rcp_f32_e32 v98, v98
	v_rcp_f32_e32 v99, v99
	v_rcp_f32_e32 v100, v100
	v_rcp_f32_e32 v101, v101
	v_rcp_f32_e32 v102, v102
	v_rcp_f32_e32 v103, v103
	s_nop 0
	v_cvt_pk_bf16_f32 v100, v100, v101
	v_cvt_pk_bf16_f32 v101, v102, v103
	v_cvt_pk_bf16_f32 v102, v96, v97
	v_cvt_pk_bf16_f32 v103, v98, v99
	global_store_dwordx4 v[112:113], v[100:103], off offset:256
	s_nop 1
	v_add_u32_e32 v106, 0x80, v150
	v_mov_b64_e32 v[104:105], s[12:13]
	v_mad_i64_i32 v[104:105], s[50:51], v106, s68, v[104:105]
	v_lshl_add_u64 v[104:105], v[152:153], 1, v[104:105]
	s_mov_b32 s50, 0xbfb8aa3b
	s_mov_b32 s52, 1.0
	v_pk_mul_f32 v[24:25], v[24:25], s[50:51] op_sel_hi:[1,0]
	v_pk_mul_f32 v[26:27], v[26:27], s[50:51] op_sel_hi:[1,0]
	v_pk_mul_f32 v[28:29], v[28:29], s[50:51] op_sel_hi:[1,0]
	v_pk_mul_f32 v[30:31], v[30:31], s[50:51] op_sel_hi:[1,0]
	v_exp_f32_e32 v24, v24
	v_exp_f32_e32 v25, v25
	v_exp_f32_e32 v26, v26
	v_exp_f32_e32 v27, v27
	v_exp_f32_e32 v28, v28
	v_exp_f32_e32 v29, v29
	v_exp_f32_e32 v30, v30
	v_exp_f32_e32 v31, v31
	v_pk_add_f32 v[24:25], v[24:25], s[52:53] op_sel_hi:[1,0]
	v_pk_add_f32 v[26:27], v[26:27], s[52:53] op_sel_hi:[1,0]
	v_pk_add_f32 v[28:29], v[28:29], s[52:53] op_sel_hi:[1,0]
	v_pk_add_f32 v[30:31], v[30:31], s[52:53] op_sel_hi:[1,0]
	v_rcp_f32_e32 v24, v24
	v_rcp_f32_e32 v25, v25
	v_rcp_f32_e32 v26, v26
	v_rcp_f32_e32 v27, v27
	v_rcp_f32_e32 v28, v28
	v_rcp_f32_e32 v29, v29
	v_rcp_f32_e32 v30, v30
	v_rcp_f32_e32 v31, v31
	s_nop 0
	v_cvt_pk_bf16_f32 v98, v28, v29
	v_cvt_pk_bf16_f32 v99, v30, v31
	v_cvt_pk_bf16_f32 v100, v24, v25
	v_cvt_pk_bf16_f32 v101, v26, v27
	global_store_dwordx4 v[104:105], v[98:101], off
	s_nop 1
	s_mov_b32 s50, 0xbfb8aa3b
	s_mov_b32 s52, 1.0
	v_pk_mul_f32 v[88:89], v[88:89], s[50:51] op_sel_hi:[1,0]
	v_pk_mul_f32 v[90:91], v[90:91], s[50:51] op_sel_hi:[1,0]
	v_pk_mul_f32 v[92:93], v[92:93], s[50:51] op_sel_hi:[1,0]
	v_pk_mul_f32 v[94:95], v[94:95], s[50:51] op_sel_hi:[1,0]
	v_exp_f32_e32 v88, v88
	v_exp_f32_e32 v89, v89
	v_exp_f32_e32 v90, v90
	v_exp_f32_e32 v91, v91
	v_exp_f32_e32 v92, v92
	v_exp_f32_e32 v93, v93
	v_exp_f32_e32 v94, v94
	v_exp_f32_e32 v95, v95
	v_pk_add_f32 v[88:89], v[88:89], s[52:53] op_sel_hi:[1,0]
	v_pk_add_f32 v[90:91], v[90:91], s[52:53] op_sel_hi:[1,0]
	v_pk_add_f32 v[92:93], v[92:93], s[52:53] op_sel_hi:[1,0]
	v_pk_add_f32 v[94:95], v[94:95], s[52:53] op_sel_hi:[1,0]
	v_rcp_f32_e32 v88, v88
	v_rcp_f32_e32 v89, v89
	v_rcp_f32_e32 v90, v90
	v_rcp_f32_e32 v91, v91
	v_rcp_f32_e32 v92, v92
	v_rcp_f32_e32 v93, v93
	v_rcp_f32_e32 v94, v94
	v_rcp_f32_e32 v95, v95
	s_nop 0
	v_cvt_pk_bf16_f32 v92, v92, v93
	v_cvt_pk_bf16_f32 v93, v94, v95
	v_cvt_pk_bf16_f32 v94, v88, v89
	v_cvt_pk_bf16_f32 v95, v90, v91
	global_store_dwordx4 v[104:105], v[92:95], off offset:256
	s_nop 1
	v_add_u32_e32 v98, 0x90, v150
	v_mov_b64_e32 v[96:97], s[12:13]
	v_mad_i64_i32 v[96:97], s[50:51], v98, s68, v[96:97]
	v_lshl_add_u64 v[96:97], v[152:153], 1, v[96:97]
	s_mov_b32 s50, 0xbfb8aa3b
	s_mov_b32 s52, 1.0
	v_pk_mul_f32 v[16:17], v[16:17], s[50:51] op_sel_hi:[1,0]
	v_pk_mul_f32 v[18:19], v[18:19], s[50:51] op_sel_hi:[1,0]
	v_pk_mul_f32 v[20:21], v[20:21], s[50:51] op_sel_hi:[1,0]
	v_pk_mul_f32 v[22:23], v[22:23], s[50:51] op_sel_hi:[1,0]
	v_exp_f32_e32 v16, v16
	v_exp_f32_e32 v17, v17
	v_exp_f32_e32 v18, v18
	v_exp_f32_e32 v19, v19
	v_exp_f32_e32 v20, v20
	v_exp_f32_e32 v21, v21
	v_exp_f32_e32 v22, v22
	v_exp_f32_e32 v23, v23
	v_pk_add_f32 v[16:17], v[16:17], s[52:53] op_sel_hi:[1,0]
	v_pk_add_f32 v[18:19], v[18:19], s[52:53] op_sel_hi:[1,0]
	v_pk_add_f32 v[20:21], v[20:21], s[52:53] op_sel_hi:[1,0]
	v_pk_add_f32 v[22:23], v[22:23], s[52:53] op_sel_hi:[1,0]
	v_rcp_f32_e32 v16, v16
	v_rcp_f32_e32 v17, v17
	v_rcp_f32_e32 v18, v18
	v_rcp_f32_e32 v19, v19
	v_rcp_f32_e32 v20, v20
	v_rcp_f32_e32 v21, v21
	v_rcp_f32_e32 v22, v22
	v_rcp_f32_e32 v23, v23
	s_nop 0
	v_cvt_pk_bf16_f32 v90, v20, v21
	v_cvt_pk_bf16_f32 v91, v22, v23
	v_cvt_pk_bf16_f32 v92, v16, v17
	v_cvt_pk_bf16_f32 v93, v18, v19
	global_store_dwordx4 v[96:97], v[90:93], off
	s_nop 1
	s_mov_b32 s50, 0xbfb8aa3b
	s_mov_b32 s52, 1.0
	v_pk_mul_f32 v[80:81], v[80:81], s[50:51] op_sel_hi:[1,0]
	v_pk_mul_f32 v[82:83], v[82:83], s[50:51] op_sel_hi:[1,0]
	v_pk_mul_f32 v[84:85], v[84:85], s[50:51] op_sel_hi:[1,0]
	v_pk_mul_f32 v[86:87], v[86:87], s[50:51] op_sel_hi:[1,0]
	v_exp_f32_e32 v80, v80
	v_exp_f32_e32 v81, v81
	v_exp_f32_e32 v82, v82
	v_exp_f32_e32 v83, v83
	v_exp_f32_e32 v84, v84
	v_exp_f32_e32 v85, v85
	v_exp_f32_e32 v86, v86
	v_exp_f32_e32 v87, v87
	v_pk_add_f32 v[80:81], v[80:81], s[52:53] op_sel_hi:[1,0]
	v_pk_add_f32 v[82:83], v[82:83], s[52:53] op_sel_hi:[1,0]
	v_pk_add_f32 v[84:85], v[84:85], s[52:53] op_sel_hi:[1,0]
	v_pk_add_f32 v[86:87], v[86:87], s[52:53] op_sel_hi:[1,0]
	v_rcp_f32_e32 v80, v80
	v_rcp_f32_e32 v81, v81
	v_rcp_f32_e32 v82, v82
	v_rcp_f32_e32 v83, v83
	v_rcp_f32_e32 v84, v84
	v_rcp_f32_e32 v85, v85
	v_rcp_f32_e32 v86, v86
	v_rcp_f32_e32 v87, v87
	s_nop 0
	v_cvt_pk_bf16_f32 v84, v84, v85
	v_cvt_pk_bf16_f32 v85, v86, v87
	v_cvt_pk_bf16_f32 v86, v80, v81
	v_cvt_pk_bf16_f32 v87, v82, v83
	global_store_dwordx4 v[96:97], v[84:87], off offset:256
	s_nop 1
	v_add_u32_e32 v90, 0xa0, v150
	v_mov_b64_e32 v[88:89], s[12:13]
	v_mad_i64_i32 v[88:89], s[50:51], v90, s68, v[88:89]
	v_lshl_add_u64 v[88:89], v[152:153], 1, v[88:89]
	s_mov_b32 s50, 0xbfb8aa3b
	s_mov_b32 s52, 1.0
	v_pk_mul_f32 v[8:9], v[8:9], s[50:51] op_sel_hi:[1,0]
	v_pk_mul_f32 v[10:11], v[10:11], s[50:51] op_sel_hi:[1,0]
	v_pk_mul_f32 v[12:13], v[12:13], s[50:51] op_sel_hi:[1,0]
	v_pk_mul_f32 v[14:15], v[14:15], s[50:51] op_sel_hi:[1,0]
	v_exp_f32_e32 v8, v8
	v_exp_f32_e32 v9, v9
	v_exp_f32_e32 v10, v10
	v_exp_f32_e32 v11, v11
	v_exp_f32_e32 v12, v12
	v_exp_f32_e32 v13, v13
	v_exp_f32_e32 v14, v14
	v_exp_f32_e32 v15, v15
	v_pk_add_f32 v[8:9], v[8:9], s[52:53] op_sel_hi:[1,0]
	v_pk_add_f32 v[10:11], v[10:11], s[52:53] op_sel_hi:[1,0]
	v_pk_add_f32 v[12:13], v[12:13], s[52:53] op_sel_hi:[1,0]
	v_pk_add_f32 v[14:15], v[14:15], s[52:53] op_sel_hi:[1,0]
	v_rcp_f32_e32 v8, v8
	v_rcp_f32_e32 v9, v9
	v_rcp_f32_e32 v10, v10
	v_rcp_f32_e32 v11, v11
	v_rcp_f32_e32 v12, v12
	v_rcp_f32_e32 v13, v13
	v_rcp_f32_e32 v14, v14
	v_rcp_f32_e32 v15, v15
	s_nop 0
	v_cvt_pk_bf16_f32 v82, v12, v13
	v_cvt_pk_bf16_f32 v83, v14, v15
	v_cvt_pk_bf16_f32 v84, v8, v9
	v_cvt_pk_bf16_f32 v85, v10, v11
	global_store_dwordx4 v[88:89], v[82:85], off
	s_nop 1
	s_mov_b32 s50, 0xbfb8aa3b
	s_mov_b32 s52, 1.0
	v_pk_mul_f32 v[72:73], v[72:73], s[50:51] op_sel_hi:[1,0]
	v_pk_mul_f32 v[74:75], v[74:75], s[50:51] op_sel_hi:[1,0]
	v_pk_mul_f32 v[76:77], v[76:77], s[50:51] op_sel_hi:[1,0]
	v_pk_mul_f32 v[78:79], v[78:79], s[50:51] op_sel_hi:[1,0]
	v_exp_f32_e32 v72, v72
	v_exp_f32_e32 v73, v73
	v_exp_f32_e32 v74, v74
	v_exp_f32_e32 v75, v75
	v_exp_f32_e32 v76, v76
	v_exp_f32_e32 v77, v77
	v_exp_f32_e32 v78, v78
	v_exp_f32_e32 v79, v79
	v_pk_add_f32 v[72:73], v[72:73], s[52:53] op_sel_hi:[1,0]
	v_pk_add_f32 v[74:75], v[74:75], s[52:53] op_sel_hi:[1,0]
	v_pk_add_f32 v[76:77], v[76:77], s[52:53] op_sel_hi:[1,0]
	v_pk_add_f32 v[78:79], v[78:79], s[52:53] op_sel_hi:[1,0]
	v_rcp_f32_e32 v72, v72
	v_rcp_f32_e32 v73, v73
	v_rcp_f32_e32 v74, v74
	v_rcp_f32_e32 v75, v75
	v_rcp_f32_e32 v76, v76
	v_rcp_f32_e32 v77, v77
	v_rcp_f32_e32 v78, v78
	v_rcp_f32_e32 v79, v79
	s_nop 0
	v_cvt_pk_bf16_f32 v80, v72, v73
	v_cvt_pk_bf16_f32 v81, v74, v75
	v_cvt_pk_bf16_f32 v82, v76, v77
	v_cvt_pk_bf16_f32 v83, v78, v79
	global_store_dwordx4 v[88:89], v[80:83], off offset:256
	s_nop 1
	v_add_u32_e32 v82, 0xb0, v150
	v_mov_b64_e32 v[80:81], s[12:13]
	v_mad_i64_i32 v[80:81], s[50:51], v82, s68, v[80:81]
	v_lshl_add_u64 v[80:81], v[152:153], 1, v[80:81]
	s_mov_b32 s50, 0xbfb8aa3b
	s_mov_b32 s52, 1.0
	v_pk_mul_f32 v[0:1], v[0:1], s[50:51] op_sel_hi:[1,0]
	v_pk_mul_f32 v[2:3], v[2:3], s[50:51] op_sel_hi:[1,0]
	v_pk_mul_f32 v[4:5], v[4:5], s[50:51] op_sel_hi:[1,0]
	v_pk_mul_f32 v[6:7], v[6:7], s[50:51] op_sel_hi:[1,0]
	v_exp_f32_e32 v0, v0
	v_exp_f32_e32 v1, v1
	v_exp_f32_e32 v2, v2
	v_exp_f32_e32 v3, v3
	v_exp_f32_e32 v4, v4
	v_exp_f32_e32 v5, v5
	v_exp_f32_e32 v6, v6
	v_exp_f32_e32 v7, v7
	v_pk_add_f32 v[0:1], v[0:1], s[52:53] op_sel_hi:[1,0]
	v_pk_add_f32 v[2:3], v[2:3], s[52:53] op_sel_hi:[1,0]
	v_pk_add_f32 v[4:5], v[4:5], s[52:53] op_sel_hi:[1,0]
	v_pk_add_f32 v[6:7], v[6:7], s[52:53] op_sel_hi:[1,0]
	v_rcp_f32_e32 v0, v0
	v_rcp_f32_e32 v1, v1
	v_rcp_f32_e32 v2, v2
	v_rcp_f32_e32 v3, v3
	v_rcp_f32_e32 v4, v4
	v_rcp_f32_e32 v5, v5
	v_rcp_f32_e32 v6, v6
	v_rcp_f32_e32 v7, v7
	s_nop 0
	v_cvt_pk_bf16_f32 v74, v4, v5
	v_cvt_pk_bf16_f32 v75, v6, v7
	v_cvt_pk_bf16_f32 v76, v0, v1
	v_cvt_pk_bf16_f32 v77, v2, v3
	global_store_dwordx4 v[80:81], v[74:77], off
	s_nop 1
	s_mov_b32 s50, 0xbfb8aa3b
	s_mov_b32 s52, 1.0
	v_pk_mul_f32 v[64:65], v[64:65], s[50:51] op_sel_hi:[1,0]
	v_pk_mul_f32 v[66:67], v[66:67], s[50:51] op_sel_hi:[1,0]
	v_pk_mul_f32 v[68:69], v[68:69], s[50:51] op_sel_hi:[1,0]
	v_pk_mul_f32 v[70:71], v[70:71], s[50:51] op_sel_hi:[1,0]
	v_exp_f32_e32 v64, v64
	v_exp_f32_e32 v65, v65
	v_exp_f32_e32 v66, v66
	v_exp_f32_e32 v67, v67
	v_exp_f32_e32 v68, v68
	v_exp_f32_e32 v69, v69
	v_exp_f32_e32 v70, v70
	v_exp_f32_e32 v71, v71
	v_pk_add_f32 v[64:65], v[64:65], s[52:53] op_sel_hi:[1,0]
	v_pk_add_f32 v[66:67], v[66:67], s[52:53] op_sel_hi:[1,0]
	v_pk_add_f32 v[68:69], v[68:69], s[52:53] op_sel_hi:[1,0]
	v_pk_add_f32 v[70:71], v[70:71], s[52:53] op_sel_hi:[1,0]
	v_rcp_f32_e32 v64, v64
	v_rcp_f32_e32 v65, v65
	v_rcp_f32_e32 v66, v66
	v_rcp_f32_e32 v67, v67
	v_rcp_f32_e32 v68, v68
	v_rcp_f32_e32 v69, v69
	v_rcp_f32_e32 v70, v70
	v_rcp_f32_e32 v71, v71
	s_nop 0
	v_cvt_pk_bf16_f32 v72, v64, v65
	v_cvt_pk_bf16_f32 v73, v66, v67
	v_cvt_pk_bf16_f32 v74, v68, v69
	v_cvt_pk_bf16_f32 v75, v70, v71
	global_store_dwordx4 v[80:81], v[72:75], off offset:256
	s_nop 1
	s_branch .LBB0_251
.Lepi_plain_0:
	v_lshl_or_b32 v152, s6, 8, v162
	v_mov_b64_e32 v[154:155], s[12:13]
	v_ashrrev_i32_e32 v153, 31, v152
	v_mad_i64_i32 v[154:155], s[6:7], v150, s68, v[154:155]
	v_lshl_add_u64 v[154:155], v[152:153], 1, v[154:155]
	v_cvt_pk_bf16_f32 v128, v60, v61
	v_cvt_pk_bf16_f32 v129, v62, v63
	v_cvt_pk_bf16_f32 v130, v56, v57
	v_cvt_pk_bf16_f32 v131, v58, v59
	global_store_dwordx4 v[154:155], v[128:131], off
	s_nop 1
	v_cvt_pk_bf16_f32 v124, v124, v125
	v_cvt_pk_bf16_f32 v125, v126, v127
	v_cvt_pk_bf16_f32 v126, v120, v121
	v_cvt_pk_bf16_f32 v127, v122, v123
	global_store_dwordx4 v[154:155], v[124:127], off offset:256
	s_nop 1
	v_or_b32_e32 v130, 16, v150
	v_mov_b64_e32 v[128:129], s[12:13]
	v_mad_i64_i32 v[128:129], s[50:51], v130, s68, v[128:129]
	v_lshl_add_u64 v[128:129], v[152:153], 1, v[128:129]
	v_cvt_pk_bf16_f32 v122, v52, v53
	v_cvt_pk_bf16_f32 v123, v54, v55
	v_cvt_pk_bf16_f32 v124, v48, v49
	v_cvt_pk_bf16_f32 v125, v50, v51
	global_store_dwordx4 v[128:129], v[122:125], off
	s_nop 1
	v_cvt_pk_bf16_f32 v116, v116, v117
	v_cvt_pk_bf16_f32 v117, v118, v119
	v_cvt_pk_bf16_f32 v118, v112, v113
	v_cvt_pk_bf16_f32 v119, v114, v115
	global_store_dwordx4 v[128:129], v[116:119], off offset:256
	s_nop 1
	v_or_b32_e32 v122, 32, v150
	v_mov_b64_e32 v[120:121], s[12:13]
	v_mad_i64_i32 v[120:121], s[50:51], v122, s68, v[120:121]
	v_lshl_add_u64 v[120:121], v[152:153], 1, v[120:121]
	v_cvt_pk_bf16_f32 v114, v44, v45
	v_cvt_pk_bf16_f32 v115, v46, v47
	v_cvt_pk_bf16_f32 v116, v40, v41
	v_cvt_pk_bf16_f32 v117, v42, v43
	global_store_dwordx4 v[120:121], v[114:117], off
	s_nop 1
	v_cvt_pk_bf16_f32 v108, v108, v109
	v_cvt_pk_bf16_f32 v109, v110, v111
	v_cvt_pk_bf16_f32 v110, v104, v105
	v_cvt_pk_bf16_f32 v111, v106, v107
	global_store_dwordx4 v[120:121], v[108:111], off offset:256
	s_nop 1
	v_or_b32_e32 v114, 48, v150
	v_mov_b64_e32 v[112:113], s[12:13]
	v_mad_i64_i32 v[112:113], s[50:51], v114, s68, v[112:113]
	v_lshl_add_u64 v[112:113], v[152:153], 1, v[112:113]
	v_cvt_pk_bf16_f32 v106, v36, v37
	v_cvt_pk_bf16_f32 v107, v38, v39
	v_cvt_pk_bf16_f32 v108, v32, v33
	v_cvt_pk_bf16_f32 v109, v34, v35
	global_store_dwordx4 v[112:113], v[106:109], off
	s_nop 1
	v_cvt_pk_bf16_f32 v100, v100, v101
	v_cvt_pk_bf16_f32 v101, v102, v103
	v_cvt_pk_bf16_f32 v102, v96, v97
	v_cvt_pk_bf16_f32 v103, v98, v99
	global_store_dwordx4 v[112:113], v[100:103], off offset:256
	s_nop 1
	v_add_u32_e32 v106, 0x80, v150
	v_mov_b64_e32 v[104:105], s[12:13]
	v_mad_i64_i32 v[104:105], s[50:51], v106, s68, v[104:105]
	v_lshl_add_u64 v[104:105], v[152:153], 1, v[104:105]
	v_cvt_pk_bf16_f32 v98, v28, v29
	v_cvt_pk_bf16_f32 v99, v30, v31
	v_cvt_pk_bf16_f32 v100, v24, v25
	v_cvt_pk_bf16_f32 v101, v26, v27
	global_store_dwordx4 v[104:105], v[98:101], off
	s_nop 1
	v_cvt_pk_bf16_f32 v92, v92, v93
	v_cvt_pk_bf16_f32 v93, v94, v95
	v_cvt_pk_bf16_f32 v94, v88, v89
	v_cvt_pk_bf16_f32 v95, v90, v91
	global_store_dwordx4 v[104:105], v[92:95], off offset:256
	s_nop 1
	v_add_u32_e32 v98, 0x90, v150
	v_mov_b64_e32 v[96:97], s[12:13]
	v_mad_i64_i32 v[96:97], s[50:51], v98, s68, v[96:97]
	v_lshl_add_u64 v[96:97], v[152:153], 1, v[96:97]
	v_cvt_pk_bf16_f32 v90, v20, v21
	v_cvt_pk_bf16_f32 v91, v22, v23
	v_cvt_pk_bf16_f32 v92, v16, v17
	v_cvt_pk_bf16_f32 v93, v18, v19
	global_store_dwordx4 v[96:97], v[90:93], off
	s_nop 1
	v_cvt_pk_bf16_f32 v84, v84, v85
	v_cvt_pk_bf16_f32 v85, v86, v87
	v_cvt_pk_bf16_f32 v86, v80, v81
	v_cvt_pk_bf16_f32 v87, v82, v83
	global_store_dwordx4 v[96:97], v[84:87], off offset:256
	s_nop 1
	v_add_u32_e32 v90, 0xa0, v150
	v_mov_b64_e32 v[88:89], s[12:13]
	v_mad_i64_i32 v[88:89], s[50:51], v90, s68, v[88:89]
	v_lshl_add_u64 v[88:89], v[152:153], 1, v[88:89]
	v_cvt_pk_bf16_f32 v82, v12, v13
	v_cvt_pk_bf16_f32 v83, v14, v15
	v_cvt_pk_bf16_f32 v84, v8, v9
	v_cvt_pk_bf16_f32 v85, v10, v11
	global_store_dwordx4 v[88:89], v[82:85], off
	s_nop 1
	v_cvt_pk_bf16_f32 v80, v72, v73
	v_cvt_pk_bf16_f32 v81, v74, v75
	v_cvt_pk_bf16_f32 v82, v76, v77
	v_cvt_pk_bf16_f32 v83, v78, v79
	global_store_dwordx4 v[88:89], v[80:83], off offset:256
	s_nop 1
	v_add_u32_e32 v82, 0xb0, v150
	v_mov_b64_e32 v[80:81], s[12:13]
	v_mad_i64_i32 v[80:81], s[50:51], v82, s68, v[80:81]
	v_lshl_add_u64 v[80:81], v[152:153], 1, v[80:81]
	v_cvt_pk_bf16_f32 v74, v4, v5
	v_cvt_pk_bf16_f32 v75, v6, v7
	v_cvt_pk_bf16_f32 v76, v0, v1
	v_cvt_pk_bf16_f32 v77, v2, v3
	global_store_dwordx4 v[80:81], v[74:77], off
	s_nop 1
	v_cvt_pk_bf16_f32 v72, v64, v65
	v_cvt_pk_bf16_f32 v73, v66, v67
	v_cvt_pk_bf16_f32 v74, v68, v69
	v_cvt_pk_bf16_f32 v75, v70, v71
	global_store_dwordx4 v[80:81], v[72:75], off offset:256
	s_nop 1
	s_branch .LBB0_251

.LBB0_1576:
	s_cmp_gt_i32 s12, 21
	s_cbranch_scc1 .Lepi_sig_1
	s_cmp_gt_i32 s12, 1
	s_cbranch_scc1 .Lepi_plain_1
	s_cmp_gt_i32 s12, 1
	v_pk_mul_f32 v[128:129], v[60:61], s[30:31] op_sel_hi:[1,0]
	s_cselect_b64 s[10:11], -1, 0
	s_cmp_lt_i32 s12, 22
	v_pk_mul_f32 v[130:131], v[62:63], s[30:31] op_sel_hi:[1,0]
	v_pk_mul_f32 v[152:153], v[58:59], s[30:31] op_sel_hi:[1,0]
	v_pk_mul_f32 v[132:133], v[56:57], s[30:31] op_sel_hi:[1,0]
	s_cselect_b64 s[42:43], -1, 0
	s_cmp_gt_i32 s12, 21
	v_cndmask_b32_e64 v128, v128, v60, s[10:11]
	v_cndmask_b32_e64 v129, v129, v61, s[10:11]
	v_cndmask_b32_e64 v130, v130, v62, s[10:11]
	v_cndmask_b32_e64 v135, v131, v63, s[10:11]
	v_cndmask_b32_e64 v132, v132, v56, s[10:11]
	v_cndmask_b32_e64 v133, v133, v57, s[10:11]
	v_cndmask_b32_e64 v134, v152, v58, s[10:11]
	v_cndmask_b32_e64 v131, v153, v59, s[10:11]
	s_mov_b64 s[44:45], -1
	s_cbranch_scc1 .LBB0_1578
	s_mov_b64 s[44:45], 0

.Lepi_sig_1:
	v_lshl_or_b32 v152, s12, 8, v162
	v_mov_b64_e32 v[154:155], s[16:17]
	v_ashrrev_i32_e32 v153, 31, v152
	v_mad_i64_i32 v[154:155], s[12:13], v150, s59, v[154:155]
	v_lshl_add_u64 v[154:155], v[152:153], 1, v[154:155]
	s_mov_b32 s42, 0xbfb8aa3b
	s_mov_b32 s44, 1.0
	v_pk_mul_f32 v[56:57], v[56:57], s[42:43] op_sel_hi:[1,0]
	v_pk_mul_f32 v[58:59], v[58:59], s[42:43] op_sel_hi:[1,0]
	v_pk_mul_f32 v[60:61], v[60:61], s[42:43] op_sel_hi:[1,0]
	v_pk_mul_f32 v[62:63], v[62:63], s[42:43] op_sel_hi:[1,0]
	v_exp_f32_e32 v56, v56
	v_exp_f32_e32 v57, v57
	v_exp_f32_e32 v58, v58
	v_exp_f32_e32 v59, v59
	v_exp_f32_e32 v60, v60
	v_exp_f32_e32 v61, v61
	v_exp_f32_e32 v62, v62
	v_exp_f32_e32 v63, v63
	v_pk_add_f32 v[56:57], v[56:57], s[44:45] op_sel_hi:[1,0]
	v_pk_add_f32 v[58:59], v[58:59], s[44:45] op_sel_hi:[1,0]
	v_pk_add_f32 v[60:61], v[60:61], s[44:45] op_sel_hi:[1,0]
	v_pk_add_f32 v[62:63], v[62:63], s[44:45] op_sel_hi:[1,0]
	v_rcp_f32_e32 v56, v56
	v_rcp_f32_e32 v57, v57
	v_rcp_f32_e32 v58, v58
	v_rcp_f32_e32 v59, v59
	v_rcp_f32_e32 v60, v60
	v_rcp_f32_e32 v61, v61
	v_rcp_f32_e32 v62, v62
	v_rcp_f32_e32 v63, v63
	s_nop 0
	v_cvt_pk_bf16_f32 v128, v60, v61
	v_cvt_pk_bf16_f32 v129, v62, v63
	v_cvt_pk_bf16_f32 v130, v56, v57
	v_cvt_pk_bf16_f32 v131, v58, v59
	global_store_dwordx4 v[154:155], v[128:131], off
	s_nop 1
	s_mov_b32 s42, 0xbfb8aa3b
	s_mov_b32 s44, 1.0
	v_pk_mul_f32 v[120:121], v[120:121], s[42:43] op_sel_hi:[1,0]
	v_pk_mul_f32 v[122:123], v[122:123], s[42:43] op_sel_hi:[1,0]
	v_pk_mul_f32 v[124:125], v[124:125], s[42:43] op_sel_hi:[1,0]
	v_pk_mul_f32 v[126:127], v[126:127], s[42:43] op_sel_hi:[1,0]
	v_exp_f32_e32 v120, v120
	v_exp_f32_e32 v121, v121
	v_exp_f32_e32 v122, v122
	v_exp_f32_e32 v123, v123
	v_exp_f32_e32 v124, v124
	v_exp_f32_e32 v125, v125
	v_exp_f32_e32 v126, v126
	v_exp_f32_e32 v127, v127
	v_pk_add_f32 v[120:121], v[120:121], s[44:45] op_sel_hi:[1,0]
	v_pk_add_f32 v[122:123], v[122:123], s[44:45] op_sel_hi:[1,0]
	v_pk_add_f32 v[124:125], v[124:125], s[44:45] op_sel_hi:[1,0]
	v_pk_add_f32 v[126:127], v[126:127], s[44:45] op_sel_hi:[1,0]
	v_rcp_f32_e32 v120, v120
	v_rcp_f32_e32 v121, v121
	v_rcp_f32_e32 v122, v122
	v_rcp_f32_e32 v123, v123
	v_rcp_f32_e32 v124, v124
	v_rcp_f32_e32 v125, v125
	v_rcp_f32_e32 v126, v126
	v_rcp_f32_e32 v127, v127
	s_nop 0
	v_cvt_pk_bf16_f32 v124, v124, v125
	v_cvt_pk_bf16_f32 v125, v126, v127
	v_cvt_pk_bf16_f32 v126, v120, v121
	v_cvt_pk_bf16_f32 v127, v122, v123
	global_store_dwordx4 v[154:155], v[124:127], off offset:256
	s_nop 1
	v_or_b32_e32 v130, 16, v150
	v_mov_b64_e32 v[128:129], s[16:17]
	v_mad_i64_i32 v[128:129], s[42:43], v130, s59, v[128:129]
	v_lshl_add_u64 v[128:129], v[152:153], 1, v[128:129]
	s_mov_b32 s42, 0xbfb8aa3b
	s_mov_b32 s44, 1.0
	v_pk_mul_f32 v[48:49], v[48:49], s[42:43] op_sel_hi:[1,0]
	v_pk_mul_f32 v[50:51], v[50:51], s[42:43] op_sel_hi:[1,0]
	v_pk_mul_f32 v[52:53], v[52:53], s[42:43] op_sel_hi:[1,0]
	v_pk_mul_f32 v[54:55], v[54:55], s[42:43] op_sel_hi:[1,0]
	v_exp_f32_e32 v48, v48
	v_exp_f32_e32 v49, v49
	v_exp_f32_e32 v50, v50
	v_exp_f32_e32 v51, v51
	v_exp_f32_e32 v52, v52
	v_exp_f32_e32 v53, v53
	v_exp_f32_e32 v54, v54
	v_exp_f32_e32 v55, v55
	v_pk_add_f32 v[48:49], v[48:49], s[44:45] op_sel_hi:[1,0]
	v_pk_add_f32 v[50:51], v[50:51], s[44:45] op_sel_hi:[1,0]
	v_pk_add_f32 v[52:53], v[52:53], s[44:45] op_sel_hi:[1,0]
	v_pk_add_f32 v[54:55], v[54:55], s[44:45] op_sel_hi:[1,0]
	v_rcp_f32_e32 v48, v48
	v_rcp_f32_e32 v49, v49
	v_rcp_f32_e32 v50, v50
	v_rcp_f32_e32 v51, v51
	v_rcp_f32_e32 v52, v52
	v_rcp_f32_e32 v53, v53
	v_rcp_f32_e32 v54, v54
	v_rcp_f32_e32 v55, v55
	s_nop 0
	v_cvt_pk_bf16_f32 v122, v52, v53
	v_cvt_pk_bf16_f32 v123, v54, v55
	v_cvt_pk_bf16_f32 v124, v48, v49
	v_cvt_pk_bf16_f32 v125, v50, v51
	global_store_dwordx4 v[128:129], v[122:125], off
	s_nop 1
	s_mov_b32 s42, 0xbfb8aa3b
	s_mov_b32 s44, 1.0
	v_pk_mul_f32 v[112:113], v[112:113], s[42:43] op_sel_hi:[1,0]
	v_pk_mul_f32 v[114:115], v[114:115], s[42:43] op_sel_hi:[1,0]
	v_pk_mul_f32 v[116:117], v[116:117], s[42:43] op_sel_hi:[1,0]
	v_pk_mul_f32 v[118:119], v[118:119], s[42:43] op_sel_hi:[1,0]
	v_exp_f32_e32 v112, v112
	v_exp_f32_e32 v113, v113
	v_exp_f32_e32 v114, v114
	v_exp_f32_e32 v115, v115
	v_exp_f32_e32 v116, v116
	v_exp_f32_e32 v117, v117
	v_exp_f32_e32 v118, v118
	v_exp_f32_e32 v119, v119
	v_pk_add_f32 v[112:113], v[112:113], s[44:45] op_sel_hi:[1,0]
	v_pk_add_f32 v[114:115], v[114:115], s[44:45] op_sel_hi:[1,0]
	v_pk_add_f32 v[116:117], v[116:117], s[44:45] op_sel_hi:[1,0]
	v_pk_add_f32 v[118:119], v[118:119], s[44:45] op_sel_hi:[1,0]
	v_rcp_f32_e32 v112, v112
	v_rcp_f32_e32 v113, v113
	v_rcp_f32_e32 v114, v114
	v_rcp_f32_e32 v115, v115
	v_rcp_f32_e32 v116, v116
	v_rcp_f32_e32 v117, v117
	v_rcp_f32_e32 v118, v118
	v_rcp_f32_e32 v119, v119
	s_nop 0
	v_cvt_pk_bf16_f32 v116, v116, v117
	v_cvt_pk_bf16_f32 v117, v118, v119
	v_cvt_pk_bf16_f32 v118, v112, v113
	v_cvt_pk_bf16_f32 v119, v114, v115
	global_store_dwordx4 v[128:129], v[116:119], off offset:256
	s_nop 1
	v_or_b32_e32 v122, 32, v150
	v_mov_b64_e32 v[120:121], s[16:17]
	v_mad_i64_i32 v[120:121], s[42:43], v122, s59, v[120:121]
	v_lshl_add_u64 v[120:121], v[152:153], 1, v[120:121]
	s_mov_b32 s42, 0xbfb8aa3b
	s_mov_b32 s44, 1.0
	v_pk_mul_f32 v[40:41], v[40:41], s[42:43] op_sel_hi:[1,0]
	v_pk_mul_f32 v[42:43], v[42:43], s[42:43] op_sel_hi:[1,0]
	v_pk_mul_f32 v[44:45], v[44:45], s[42:43] op_sel_hi:[1,0]
	v_pk_mul_f32 v[46:47], v[46:47], s[42:43] op_sel_hi:[1,0]
	v_exp_f32_e32 v40, v40
	v_exp_f32_e32 v41, v41
	v_exp_f32_e32 v42, v42
	v_exp_f32_e32 v43, v43
	v_exp_f32_e32 v44, v44
	v_exp_f32_e32 v45, v45
	v_exp_f32_e32 v46, v46
	v_exp_f32_e32 v47, v47
	v_pk_add_f32 v[40:41], v[40:41], s[44:45] op_sel_hi:[1,0]
	v_pk_add_f32 v[42:43], v[42:43], s[44:45] op_sel_hi:[1,0]
	v_pk_add_f32 v[44:45], v[44:45], s[44:45] op_sel_hi:[1,0]
	v_pk_add_f32 v[46:47], v[46:47], s[44:45] op_sel_hi:[1,0]
	v_rcp_f32_e32 v40, v40
	v_rcp_f32_e32 v41, v41
	v_rcp_f32_e32 v42, v42
	v_rcp_f32_e32 v43, v43
	v_rcp_f32_e32 v44, v44
	v_rcp_f32_e32 v45, v45
	v_rcp_f32_e32 v46, v46
	v_rcp_f32_e32 v47, v47
	s_nop 0
	v_cvt_pk_bf16_f32 v114, v44, v45
	v_cvt_pk_bf16_f32 v115, v46, v47
	v_cvt_pk_bf16_f32 v116, v40, v41
	v_cvt_pk_bf16_f32 v117, v42, v43
	global_store_dwordx4 v[120:121], v[114:117], off
	s_nop 1
	s_mov_b32 s42, 0xbfb8aa3b
	s_mov_b32 s44, 1.0
	v_pk_mul_f32 v[104:105], v[104:105], s[42:43] op_sel_hi:[1,0]
	v_pk_mul_f32 v[106:107], v[106:107], s[42:43] op_sel_hi:[1,0]
	v_pk_mul_f32 v[108:109], v[108:109], s[42:43] op_sel_hi:[1,0]
	v_pk_mul_f32 v[110:111], v[110:111], s[42:43] op_sel_hi:[1,0]
	v_exp_f32_e32 v104, v104
	v_exp_f32_e32 v105, v105
	v_exp_f32_e32 v106, v106
	v_exp_f32_e32 v107, v107
	v_exp_f32_e32 v108, v108
	v_exp_f32_e32 v109, v109
	v_exp_f32_e32 v110, v110
	v_exp_f32_e32 v111, v111
	v_pk_add_f32 v[104:105], v[104:105], s[44:45] op_sel_hi:[1,0]
	v_pk_add_f32 v[106:107], v[106:107], s[44:45] op_sel_hi:[1,0]
	v_pk_add_f32 v[108:109], v[108:109], s[44:45] op_sel_hi:[1,0]
	v_pk_add_f32 v[110:111], v[110:111], s[44:45] op_sel_hi:[1,0]
	v_rcp_f32_e32 v104, v104
	v_rcp_f32_e32 v105, v105
	v_rcp_f32_e32 v106, v106
	v_rcp_f32_e32 v107, v107
	v_rcp_f32_e32 v108, v108
	v_rcp_f32_e32 v109, v109
	v_rcp_f32_e32 v110, v110
	v_rcp_f32_e32 v111, v111
	s_nop 0
	v_cvt_pk_bf16_f32 v108, v108, v109
	v_cvt_pk_bf16_f32 v109, v110, v111
	v_cvt_pk_bf16_f32 v110, v104, v105
	v_cvt_pk_bf16_f32 v111, v106, v107
	global_store_dwordx4 v[120:121], v[108:111], off offset:256
	s_nop 1
	v_or_b32_e32 v114, 48, v150
	v_mov_b64_e32 v[112:113], s[16:17]
	v_mad_i64_i32 v[112:113], s[42:43], v114, s59, v[112:113]
	v_lshl_add_u64 v[112:113], v[152:153], 1, v[112:113]
	s_mov_b32 s42, 0xbfb8aa3b
	s_mov_b32 s44, 1.0
	v_pk_mul_f32 v[32:33], v[32:33], s[42:43] op_sel_hi:[1,0]
	v_pk_mul_f32 v[34:35], v[34:35], s[42:43] op_sel_hi:[1,0]
	v_pk_mul_f32 v[36:37], v[36:37], s[42:43] op_sel_hi:[1,0]
	v_pk_mul_f32 v[38:39], v[38:39], s[42:43] op_sel_hi:[1,0]
	v_exp_f32_e32 v32, v32
	v_exp_f32_e32 v33, v33
	v_exp_f32_e32 v34, v34
	v_exp_f32_e32 v35, v35
	v_exp_f32_e32 v36, v36
	v_exp_f32_e32 v37, v37
	v_exp_f32_e32 v38, v38
	v_exp_f32_e32 v39, v39
	v_pk_add_f32 v[32:33], v[32:33], s[44:45] op_sel_hi:[1,0]
	v_pk_add_f32 v[34:35], v[34:35], s[44:45] op_sel_hi:[1,0]
	v_pk_add_f32 v[36:37], v[36:37], s[44:45] op_sel_hi:[1,0]
	v_pk_add_f32 v[38:39], v[38:39], s[44:45] op_sel_hi:[1,0]
	v_rcp_f32_e32 v32, v32
	v_rcp_f32_e32 v33, v33
	v_rcp_f32_e32 v34, v34
	v_rcp_f32_e32 v35, v35
	v_rcp_f32_e32 v36, v36
	v_rcp_f32_e32 v37, v37
	v_rcp_f32_e32 v38, v38
	v_rcp_f32_e32 v39, v39
	s_nop 0
	v_cvt_pk_bf16_f32 v106, v36, v37
	v_cvt_pk_bf16_f32 v107, v38, v39
	v_cvt_pk_bf16_f32 v108, v32, v33
	v_cvt_pk_bf16_f32 v109, v34, v35
	global_store_dwordx4 v[112:113], v[106:109], off
	s_nop 1
	s_mov_b32 s42, 0xbfb8aa3b
	s_mov_b32 s44, 1.0
	v_pk_mul_f32 v[96:97], v[96:97], s[42:43] op_sel_hi:[1,0]
	v_pk_mul_f32 v[98:99], v[98:99], s[42:43] op_sel_hi:[1,0]
	v_pk_mul_f32 v[100:101], v[100:101], s[42:43] op_sel_hi:[1,0]
	v_pk_mul_f32 v[102:103], v[102:103], s[42:43] op_sel_hi:[1,0]
	v_exp_f32_e32 v96, v96
	v_exp_f32_e32 v97, v97
	v_exp_f32_e32 v98, v98
	v_exp_f32_e32 v99, v99
	v_exp_f32_e32 v100, v100
	v_exp_f32_e32 v101, v101
	v_exp_f32_e32 v102, v102
	v_exp_f32_e32 v103, v103
	v_pk_add_f32 v[96:97], v[96:97], s[44:45] op_sel_hi:[1,0]
	v_pk_add_f32 v[98:99], v[98:99], s[44:45] op_sel_hi:[1,0]
	v_pk_add_f32 v[100:101], v[100:101], s[44:45] op_sel_hi:[1,0]
	v_pk_add_f32 v[102:103], v[102:103], s[44:45] op_sel_hi:[1,0]
	v_rcp_f32_e32 v96, v96
	v_rcp_f32_e32 v97, v97
	v_rcp_f32_e32 v98, v98
	v_rcp_f32_e32 v99, v99
	v_rcp_f32_e32 v100, v100
	v_rcp_f32_e32 v101, v101
	v_rcp_f32_e32 v102, v102
	v_rcp_f32_e32 v103, v103
	s_nop 0
	v_cvt_pk_bf16_f32 v100, v100, v101
	v_cvt_pk_bf16_f32 v101, v102, v103
	v_cvt_pk_bf16_f32 v102, v96, v97
	v_cvt_pk_bf16_f32 v103, v98, v99
	global_store_dwordx4 v[112:113], v[100:103], off offset:256
	s_nop 1
	v_add_u32_e32 v106, 0x80, v150
	v_mov_b64_e32 v[104:105], s[16:17]
	v_mad_i64_i32 v[104:105], s[42:43], v106, s59, v[104:105]
	v_lshl_add_u64 v[104:105], v[152:153], 1, v[104:105]
	s_mov_b32 s42, 0xbfb8aa3b
	s_mov_b32 s44, 1.0
	v_pk_mul_f32 v[24:25], v[24:25], s[42:43] op_sel_hi:[1,0]
	v_pk_mul_f32 v[26:27], v[26:27], s[42:43] op_sel_hi:[1,0]
	v_pk_mul_f32 v[28:29], v[28:29], s[42:43] op_sel_hi:[1,0]
	v_pk_mul_f32 v[30:31], v[30:31], s[42:43] op_sel_hi:[1,0]
	v_exp_f32_e32 v24, v24
	v_exp_f32_e32 v25, v25
	v_exp_f32_e32 v26, v26
	v_exp_f32_e32 v27, v27
	v_exp_f32_e32 v28, v28
	v_exp_f32_e32 v29, v29
	v_exp_f32_e32 v30, v30
	v_exp_f32_e32 v31, v31
	v_pk_add_f32 v[24:25], v[24:25], s[44:45] op_sel_hi:[1,0]
	v_pk_add_f32 v[26:27], v[26:27], s[44:45] op_sel_hi:[1,0]
	v_pk_add_f32 v[28:29], v[28:29], s[44:45] op_sel_hi:[1,0]
	v_pk_add_f32 v[30:31], v[30:31], s[44:45] op_sel_hi:[1,0]
	v_rcp_f32_e32 v24, v24
	v_rcp_f32_e32 v25, v25
	v_rcp_f32_e32 v26, v26
	v_rcp_f32_e32 v27, v27
	v_rcp_f32_e32 v28, v28
	v_rcp_f32_e32 v29, v29
	v_rcp_f32_e32 v30, v30
	v_rcp_f32_e32 v31, v31
	s_nop 0
	v_cvt_pk_bf16_f32 v98, v28, v29
	v_cvt_pk_bf16_f32 v99, v30, v31
	v_cvt_pk_bf16_f32 v100, v24, v25
	v_cvt_pk_bf16_f32 v101, v26, v27
	global_store_dwordx4 v[104:105], v[98:101], off
	s_nop 1
	s_mov_b32 s42, 0xbfb8aa3b
	s_mov_b32 s44, 1.0
	v_pk_mul_f32 v[88:89], v[88:89], s[42:43] op_sel_hi:[1,0]
	v_pk_mul_f32 v[90:91], v[90:91], s[42:43] op_sel_hi:[1,0]
	v_pk_mul_f32 v[92:93], v[92:93], s[42:43] op_sel_hi:[1,0]
	v_pk_mul_f32 v[94:95], v[94:95], s[42:43] op_sel_hi:[1,0]
	v_exp_f32_e32 v88, v88
	v_exp_f32_e32 v89, v89
	v_exp_f32_e32 v90, v90
	v_exp_f32_e32 v91, v91
	v_exp_f32_e32 v92, v92
	v_exp_f32_e32 v93, v93
	v_exp_f32_e32 v94, v94
	v_exp_f32_e32 v95, v95
	v_pk_add_f32 v[88:89], v[88:89], s[44:45] op_sel_hi:[1,0]
	v_pk_add_f32 v[90:91], v[90:91], s[44:45] op_sel_hi:[1,0]
	v_pk_add_f32 v[92:93], v[92:93], s[44:45] op_sel_hi:[1,0]
	v_pk_add_f32 v[94:95], v[94:95], s[44:45] op_sel_hi:[1,0]
	v_rcp_f32_e32 v88, v88
	v_rcp_f32_e32 v89, v89
	v_rcp_f32_e32 v90, v90
	v_rcp_f32_e32 v91, v91
	v_rcp_f32_e32 v92, v92
	v_rcp_f32_e32 v93, v93
	v_rcp_f32_e32 v94, v94
	v_rcp_f32_e32 v95, v95
	s_nop 0
	v_cvt_pk_bf16_f32 v92, v92, v93
	v_cvt_pk_bf16_f32 v93, v94, v95
	v_cvt_pk_bf16_f32 v94, v88, v89
	v_cvt_pk_bf16_f32 v95, v90, v91
	global_store_dwordx4 v[104:105], v[92:95], off offset:256
	s_nop 1
	v_add_u32_e32 v98, 0x90, v150
	v_mov_b64_e32 v[96:97], s[16:17]
	v_mad_i64_i32 v[96:97], s[42:43], v98, s59, v[96:97]
	v_lshl_add_u64 v[96:97], v[152:153], 1, v[96:97]
	s_mov_b32 s42, 0xbfb8aa3b
	s_mov_b32 s44, 1.0
	v_pk_mul_f32 v[16:17], v[16:17], s[42:43] op_sel_hi:[1,0]
	v_pk_mul_f32 v[18:19], v[18:19], s[42:43] op_sel_hi:[1,0]
	v_pk_mul_f32 v[20:21], v[20:21], s[42:43] op_sel_hi:[1,0]
	v_pk_mul_f32 v[22:23], v[22:23], s[42:43] op_sel_hi:[1,0]
	v_exp_f32_e32 v16, v16
	v_exp_f32_e32 v17, v17
	v_exp_f32_e32 v18, v18
	v_exp_f32_e32 v19, v19
	v_exp_f32_e32 v20, v20
	v_exp_f32_e32 v21, v21
	v_exp_f32_e32 v22, v22
	v_exp_f32_e32 v23, v23
	v_pk_add_f32 v[16:17], v[16:17], s[44:45] op_sel_hi:[1,0]
	v_pk_add_f32 v[18:19], v[18:19], s[44:45] op_sel_hi:[1,0]
	v_pk_add_f32 v[20:21], v[20:21], s[44:45] op_sel_hi:[1,0]
	v_pk_add_f32 v[22:23], v[22:23], s[44:45] op_sel_hi:[1,0]
	v_rcp_f32_e32 v16, v16
	v_rcp_f32_e32 v17, v17
	v_rcp_f32_e32 v18, v18
	v_rcp_f32_e32 v19, v19
	v_rcp_f32_e32 v20, v20
	v_rcp_f32_e32 v21, v21
	v_rcp_f32_e32 v22, v22
	v_rcp_f32_e32 v23, v23
	s_nop 0
	v_cvt_pk_bf16_f32 v90, v20, v21
	v_cvt_pk_bf16_f32 v91, v22, v23
	v_cvt_pk_bf16_f32 v92, v16, v17
	v_cvt_pk_bf16_f32 v93, v18, v19
	global_store_dwordx4 v[96:97], v[90:93], off
	s_nop 1
	s_mov_b32 s42, 0xbfb8aa3b
	s_mov_b32 s44, 1.0
	v_pk_mul_f32 v[80:81], v[80:81], s[42:43] op_sel_hi:[1,0]
	v_pk_mul_f32 v[82:83], v[82:83], s[42:43] op_sel_hi:[1,0]
	v_pk_mul_f32 v[84:85], v[84:85], s[42:43] op_sel_hi:[1,0]
	v_pk_mul_f32 v[86:87], v[86:87], s[42:43] op_sel_hi:[1,0]
	v_exp_f32_e32 v80, v80
	v_exp_f32_e32 v81, v81
	v_exp_f32_e32 v82, v82
	v_exp_f32_e32 v83, v83
	v_exp_f32_e32 v84, v84
	v_exp_f32_e32 v85, v85
	v_exp_f32_e32 v86, v86
	v_exp_f32_e32 v87, v87
	v_pk_add_f32 v[80:81], v[80:81], s[44:45] op_sel_hi:[1,0]
	v_pk_add_f32 v[82:83], v[82:83], s[44:45] op_sel_hi:[1,0]
	v_pk_add_f32 v[84:85], v[84:85], s[44:45] op_sel_hi:[1,0]
	v_pk_add_f32 v[86:87], v[86:87], s[44:45] op_sel_hi:[1,0]
	v_rcp_f32_e32 v80, v80
	v_rcp_f32_e32 v81, v81
	v_rcp_f32_e32 v82, v82
	v_rcp_f32_e32 v83, v83
	v_rcp_f32_e32 v84, v84
	v_rcp_f32_e32 v85, v85
	v_rcp_f32_e32 v86, v86
	v_rcp_f32_e32 v87, v87
	s_nop 0
	v_cvt_pk_bf16_f32 v84, v84, v85
	v_cvt_pk_bf16_f32 v85, v86, v87
	v_cvt_pk_bf16_f32 v86, v80, v81
	v_cvt_pk_bf16_f32 v87, v82, v83
	global_store_dwordx4 v[96:97], v[84:87], off offset:256
	s_nop 1
	v_add_u32_e32 v90, 0xa0, v150
	v_mov_b64_e32 v[88:89], s[16:17]
	v_mad_i64_i32 v[88:89], s[42:43], v90, s59, v[88:89]
	v_lshl_add_u64 v[88:89], v[152:153], 1, v[88:89]
	s_mov_b32 s42, 0xbfb8aa3b
	s_mov_b32 s44, 1.0
	v_pk_mul_f32 v[8:9], v[8:9], s[42:43] op_sel_hi:[1,0]
	v_pk_mul_f32 v[10:11], v[10:11], s[42:43] op_sel_hi:[1,0]
	v_pk_mul_f32 v[12:13], v[12:13], s[42:43] op_sel_hi:[1,0]
	v_pk_mul_f32 v[14:15], v[14:15], s[42:43] op_sel_hi:[1,0]
	v_exp_f32_e32 v8, v8
	v_exp_f32_e32 v9, v9
	v_exp_f32_e32 v10, v10
	v_exp_f32_e32 v11, v11
	v_exp_f32_e32 v12, v12
	v_exp_f32_e32 v13, v13
	v_exp_f32_e32 v14, v14
	v_exp_f32_e32 v15, v15
	v_pk_add_f32 v[8:9], v[8:9], s[44:45] op_sel_hi:[1,0]
	v_pk_add_f32 v[10:11], v[10:11], s[44:45] op_sel_hi:[1,0]
	v_pk_add_f32 v[12:13], v[12:13], s[44:45] op_sel_hi:[1,0]
	v_pk_add_f32 v[14:15], v[14:15], s[44:45] op_sel_hi:[1,0]
	v_rcp_f32_e32 v8, v8
	v_rcp_f32_e32 v9, v9
	v_rcp_f32_e32 v10, v10
	v_rcp_f32_e32 v11, v11
	v_rcp_f32_e32 v12, v12
	v_rcp_f32_e32 v13, v13
	v_rcp_f32_e32 v14, v14
	v_rcp_f32_e32 v15, v15
	s_nop 0
	v_cvt_pk_bf16_f32 v82, v12, v13
	v_cvt_pk_bf16_f32 v83, v14, v15
	v_cvt_pk_bf16_f32 v84, v8, v9
	v_cvt_pk_bf16_f32 v85, v10, v11
	global_store_dwordx4 v[88:89], v[82:85], off
	s_nop 1
	s_mov_b32 s42, 0xbfb8aa3b
	s_mov_b32 s44, 1.0
	v_pk_mul_f32 v[72:73], v[72:73], s[42:43] op_sel_hi:[1,0]
	v_pk_mul_f32 v[74:75], v[74:75], s[42:43] op_sel_hi:[1,0]
	v_pk_mul_f32 v[76:77], v[76:77], s[42:43] op_sel_hi:[1,0]
	v_pk_mul_f32 v[78:79], v[78:79], s[42:43] op_sel_hi:[1,0]
	v_exp_f32_e32 v72, v72
	v_exp_f32_e32 v73, v73
	v_exp_f32_e32 v74, v74
	v_exp_f32_e32 v75, v75
	v_exp_f32_e32 v76, v76
	v_exp_f32_e32 v77, v77
	v_exp_f32_e32 v78, v78
	v_exp_f32_e32 v79, v79
	v_pk_add_f32 v[72:73], v[72:73], s[44:45] op_sel_hi:[1,0]
	v_pk_add_f32 v[74:75], v[74:75], s[44:45] op_sel_hi:[1,0]
	v_pk_add_f32 v[76:77], v[76:77], s[44:45] op_sel_hi:[1,0]
	v_pk_add_f32 v[78:79], v[78:79], s[44:45] op_sel_hi:[1,0]
	v_rcp_f32_e32 v72, v72
	v_rcp_f32_e32 v73, v73
	v_rcp_f32_e32 v74, v74
	v_rcp_f32_e32 v75, v75
	v_rcp_f32_e32 v76, v76
	v_rcp_f32_e32 v77, v77
	v_rcp_f32_e32 v78, v78
	v_rcp_f32_e32 v79, v79
	s_nop 0
	v_cvt_pk_bf16_f32 v80, v72, v73
	v_cvt_pk_bf16_f32 v81, v74, v75
	v_cvt_pk_bf16_f32 v82, v76, v77
	v_cvt_pk_bf16_f32 v83, v78, v79
	global_store_dwordx4 v[88:89], v[80:83], off offset:256
	s_nop 1
	v_add_u32_e32 v82, 0xb0, v150
	v_mov_b64_e32 v[80:81], s[16:17]
	v_mad_i64_i32 v[80:81], s[42:43], v82, s59, v[80:81]
	v_lshl_add_u64 v[80:81], v[152:153], 1, v[80:81]
	s_mov_b32 s42, 0xbfb8aa3b
	s_mov_b32 s44, 1.0
	v_pk_mul_f32 v[0:1], v[0:1], s[42:43] op_sel_hi:[1,0]
	v_pk_mul_f32 v[2:3], v[2:3], s[42:43] op_sel_hi:[1,0]
	v_pk_mul_f32 v[4:5], v[4:5], s[42:43] op_sel_hi:[1,0]
	v_pk_mul_f32 v[6:7], v[6:7], s[42:43] op_sel_hi:[1,0]
	v_exp_f32_e32 v0, v0
	v_exp_f32_e32 v1, v1
	v_exp_f32_e32 v2, v2
	v_exp_f32_e32 v3, v3
	v_exp_f32_e32 v4, v4
	v_exp_f32_e32 v5, v5
	v_exp_f32_e32 v6, v6
	v_exp_f32_e32 v7, v7
	v_pk_add_f32 v[0:1], v[0:1], s[44:45] op_sel_hi:[1,0]
	v_pk_add_f32 v[2:3], v[2:3], s[44:45] op_sel_hi:[1,0]
	v_pk_add_f32 v[4:5], v[4:5], s[44:45] op_sel_hi:[1,0]
	v_pk_add_f32 v[6:7], v[6:7], s[44:45] op_sel_hi:[1,0]
	v_rcp_f32_e32 v0, v0
	v_rcp_f32_e32 v1, v1
	v_rcp_f32_e32 v2, v2
	v_rcp_f32_e32 v3, v3
	v_rcp_f32_e32 v4, v4
	v_rcp_f32_e32 v5, v5
	v_rcp_f32_e32 v6, v6
	v_rcp_f32_e32 v7, v7
	s_nop 0
	v_cvt_pk_bf16_f32 v74, v4, v5
	v_cvt_pk_bf16_f32 v75, v6, v7
	v_cvt_pk_bf16_f32 v76, v0, v1
	v_cvt_pk_bf16_f32 v77, v2, v3
	global_store_dwordx4 v[80:81], v[74:77], off
	s_nop 1
	s_mov_b32 s42, 0xbfb8aa3b
	s_mov_b32 s44, 1.0
	v_pk_mul_f32 v[64:65], v[64:65], s[42:43] op_sel_hi:[1,0]
	v_pk_mul_f32 v[66:67], v[66:67], s[42:43] op_sel_hi:[1,0]
	v_pk_mul_f32 v[68:69], v[68:69], s[42:43] op_sel_hi:[1,0]
	v_pk_mul_f32 v[70:71], v[70:71], s[42:43] op_sel_hi:[1,0]
	v_exp_f32_e32 v64, v64
	v_exp_f32_e32 v65, v65
	v_exp_f32_e32 v66, v66
	v_exp_f32_e32 v67, v67
	v_exp_f32_e32 v68, v68
	v_exp_f32_e32 v69, v69
	v_exp_f32_e32 v70, v70
	v_exp_f32_e32 v71, v71
	v_pk_add_f32 v[64:65], v[64:65], s[44:45] op_sel_hi:[1,0]
	v_pk_add_f32 v[66:67], v[66:67], s[44:45] op_sel_hi:[1,0]
	v_pk_add_f32 v[68:69], v[68:69], s[44:45] op_sel_hi:[1,0]
	v_pk_add_f32 v[70:71], v[70:71], s[44:45] op_sel_hi:[1,0]
	v_rcp_f32_e32 v64, v64
	v_rcp_f32_e32 v65, v65
	v_rcp_f32_e32 v66, v66
	v_rcp_f32_e32 v67, v67
	v_rcp_f32_e32 v68, v68
	v_rcp_f32_e32 v69, v69
	v_rcp_f32_e32 v70, v70
	v_rcp_f32_e32 v71, v71
	s_nop 0
	v_cvt_pk_bf16_f32 v72, v64, v65
	v_cvt_pk_bf16_f32 v73, v66, v67
	v_cvt_pk_bf16_f32 v74, v68, v69
	v_cvt_pk_bf16_f32 v75, v70, v71
	global_store_dwordx4 v[80:81], v[72:75], off offset:256
	s_nop 1
	s_branch .LBB0_1642
.Lepi_plain_1:
	v_lshl_or_b32 v152, s12, 8, v162
	v_mov_b64_e32 v[154:155], s[16:17]
	v_ashrrev_i32_e32 v153, 31, v152
	v_mad_i64_i32 v[154:155], s[12:13], v150, s59, v[154:155]
	v_lshl_add_u64 v[154:155], v[152:153], 1, v[154:155]
	v_cvt_pk_bf16_f32 v128, v60, v61
	v_cvt_pk_bf16_f32 v129, v62, v63
	v_cvt_pk_bf16_f32 v130, v56, v57
	v_cvt_pk_bf16_f32 v131, v58, v59
	global_store_dwordx4 v[154:155], v[128:131], off
	s_nop 1
	v_cvt_pk_bf16_f32 v124, v124, v125
	v_cvt_pk_bf16_f32 v125, v126, v127
	v_cvt_pk_bf16_f32 v126, v120, v121
	v_cvt_pk_bf16_f32 v127, v122, v123
	global_store_dwordx4 v[154:155], v[124:127], off offset:256
	s_nop 1
	v_or_b32_e32 v130, 16, v150
	v_mov_b64_e32 v[128:129], s[16:17]
	v_mad_i64_i32 v[128:129], s[42:43], v130, s59, v[128:129]
	v_lshl_add_u64 v[128:129], v[152:153], 1, v[128:129]
	v_cvt_pk_bf16_f32 v122, v52, v53
	v_cvt_pk_bf16_f32 v123, v54, v55
	v_cvt_pk_bf16_f32 v124, v48, v49
	v_cvt_pk_bf16_f32 v125, v50, v51
	global_store_dwordx4 v[128:129], v[122:125], off
	s_nop 1
	v_cvt_pk_bf16_f32 v116, v116, v117
	v_cvt_pk_bf16_f32 v117, v118, v119
	v_cvt_pk_bf16_f32 v118, v112, v113
	v_cvt_pk_bf16_f32 v119, v114, v115
	global_store_dwordx4 v[128:129], v[116:119], off offset:256
	s_nop 1
	v_or_b32_e32 v122, 32, v150
	v_mov_b64_e32 v[120:121], s[16:17]
	v_mad_i64_i32 v[120:121], s[42:43], v122, s59, v[120:121]
	v_lshl_add_u64 v[120:121], v[152:153], 1, v[120:121]
	v_cvt_pk_bf16_f32 v114, v44, v45
	v_cvt_pk_bf16_f32 v115, v46, v47
	v_cvt_pk_bf16_f32 v116, v40, v41
	v_cvt_pk_bf16_f32 v117, v42, v43
	global_store_dwordx4 v[120:121], v[114:117], off
	s_nop 1
	v_cvt_pk_bf16_f32 v108, v108, v109
	v_cvt_pk_bf16_f32 v109, v110, v111
	v_cvt_pk_bf16_f32 v110, v104, v105
	v_cvt_pk_bf16_f32 v111, v106, v107
	global_store_dwordx4 v[120:121], v[108:111], off offset:256
	s_nop 1
	v_or_b32_e32 v114, 48, v150
	v_mov_b64_e32 v[112:113], s[16:17]
	v_mad_i64_i32 v[112:113], s[42:43], v114, s59, v[112:113]
	v_lshl_add_u64 v[112:113], v[152:153], 1, v[112:113]
	v_cvt_pk_bf16_f32 v106, v36, v37
	v_cvt_pk_bf16_f32 v107, v38, v39
	v_cvt_pk_bf16_f32 v108, v32, v33
	v_cvt_pk_bf16_f32 v109, v34, v35
	global_store_dwordx4 v[112:113], v[106:109], off
	s_nop 1
	v_cvt_pk_bf16_f32 v100, v100, v101
	v_cvt_pk_bf16_f32 v101, v102, v103
	v_cvt_pk_bf16_f32 v102, v96, v97
	v_cvt_pk_bf16_f32 v103, v98, v99
	global_store_dwordx4 v[112:113], v[100:103], off offset:256
	s_nop 1
	v_add_u32_e32 v106, 0x80, v150
	v_mov_b64_e32 v[104:105], s[16:17]
	v_mad_i64_i32 v[104:105], s[42:43], v106, s59, v[104:105]
	v_lshl_add_u64 v[104:105], v[152:153], 1, v[104:105]
	v_cvt_pk_bf16_f32 v98, v28, v29
	v_cvt_pk_bf16_f32 v99, v30, v31
	v_cvt_pk_bf16_f32 v100, v24, v25
	v_cvt_pk_bf16_f32 v101, v26, v27
	global_store_dwordx4 v[104:105], v[98:101], off
	s_nop 1
	v_cvt_pk_bf16_f32 v92, v92, v93
	v_cvt_pk_bf16_f32 v93, v94, v95
	v_cvt_pk_bf16_f32 v94, v88, v89
	v_cvt_pk_bf16_f32 v95, v90, v91
	global_store_dwordx4 v[104:105], v[92:95], off offset:256
	s_nop 1
	v_add_u32_e32 v98, 0x90, v150
	v_mov_b64_e32 v[96:97], s[16:17]
	v_mad_i64_i32 v[96:97], s[42:43], v98, s59, v[96:97]
	v_lshl_add_u64 v[96:97], v[152:153], 1, v[96:97]
	v_cvt_pk_bf16_f32 v90, v20, v21
	v_cvt_pk_bf16_f32 v91, v22, v23
	v_cvt_pk_bf16_f32 v92, v16, v17
	v_cvt_pk_bf16_f32 v93, v18, v19
	global_store_dwordx4 v[96:97], v[90:93], off
	s_nop 1
	v_cvt_pk_bf16_f32 v84, v84, v85
	v_cvt_pk_bf16_f32 v85, v86, v87
	v_cvt_pk_bf16_f32 v86, v80, v81
	v_cvt_pk_bf16_f32 v87, v82, v83
	global_store_dwordx4 v[96:97], v[84:87], off offset:256
	s_nop 1
	v_add_u32_e32 v90, 0xa0, v150
	v_mov_b64_e32 v[88:89], s[16:17]
	v_mad_i64_i32 v[88:89], s[42:43], v90, s59, v[88:89]
	v_lshl_add_u64 v[88:89], v[152:153], 1, v[88:89]
	v_cvt_pk_bf16_f32 v82, v12, v13
	v_cvt_pk_bf16_f32 v83, v14, v15
	v_cvt_pk_bf16_f32 v84, v8, v9
	v_cvt_pk_bf16_f32 v85, v10, v11
	global_store_dwordx4 v[88:89], v[82:85], off
	s_nop 1
	v_cvt_pk_bf16_f32 v80, v72, v73
	v_cvt_pk_bf16_f32 v81, v74, v75
	v_cvt_pk_bf16_f32 v82, v76, v77
	v_cvt_pk_bf16_f32 v83, v78, v79
	global_store_dwordx4 v[88:89], v[80:83], off offset:256
	s_nop 1
	v_add_u32_e32 v82, 0xb0, v150
	v_mov_b64_e32 v[80:81], s[16:17]
	v_mad_i64_i32 v[80:81], s[42:43], v82, s59, v[80:81]
	v_lshl_add_u64 v[80:81], v[152:153], 1, v[80:81]
	v_cvt_pk_bf16_f32 v74, v4, v5
	v_cvt_pk_bf16_f32 v75, v6, v7
	v_cvt_pk_bf16_f32 v76, v0, v1
	v_cvt_pk_bf16_f32 v77, v2, v3
	global_store_dwordx4 v[80:81], v[74:77], off
	s_nop 1
	v_cvt_pk_bf16_f32 v72, v64, v65
	v_cvt_pk_bf16_f32 v73, v66, v67
	v_cvt_pk_bf16_f32 v74, v68, v69
	v_cvt_pk_bf16_f32 v75, v70, v71
	global_store_dwordx4 v[80:81], v[72:75], off offset:256
	s_nop 1
	s_branch .LBB0_1642
